# P8 logits/X2N loop: 37 of an iteration's 40 loads issued together at the iteration top into own registers, counted waits + copies at the old load sites (one L2 round trip per iteration instead of per
# speedup vs baseline: 1.0309x; 1.0013x over previous
.LBB0_1272:
	v_lshl_add_u64 v[22:23], s[6:7], 0, v[14:15]
	v_lshl_add_u64 v[24:25], v[12:13], 0, s[12:13]
	global_load_dwordx4 v[34:37], v[22:23], off offset:-256
	global_load_dwordx4 v[38:41], v[24:25], off
	global_load_dwordx4 v[42:45], v[24:25], off offset:16
	v_mov_b32_e32 v46, 0
	v_mov_b32_e32 v47, 0
	v_lshl_add_u64 v[30:31], s[6:7], 0, v[10:11]
	v_add_co_u32_e32 v28, vcc, s21, v30
	v_lshl_add_u64 v[26:27], s[6:7], 0, v[16:17]
	s_nop 0
	v_addc_co_u32_e32 v29, vcc, 0, v31, vcc
	v_add_co_u32_e32 v30, vcc, s22, v30
	v_mov_b32_e32 v54, 0
	s_nop 0
	v_addc_co_u32_e32 v31, vcc, 0, v31, vcc
	global_load_dwordx4 v[70:73], v[28:29], off
	global_load_dwordx4 v[74:77], v[30:31], off
	global_load_dwordx4 v[78:81], v[22:23], off offset:-192
	global_load_dwordx4 v[82:85], v[24:25], off offset:128
	global_load_dwordx4 v[86:89], v[24:25], off offset:144
	global_load_dwordx4 v[90:93], v[28:29], off offset:64
	global_load_dwordx4 v[94:97], v[30:31], off offset:64
	global_load_dwordx4 v[98:101], v[22:23], off offset:-128
	global_load_dwordx4 v[102:105], v[24:25], off offset:256
	global_load_dwordx4 v[106:109], v[24:25], off offset:272
	global_load_dwordx4 v[110:113], v[28:29], off offset:128
	global_load_dwordx4 v[114:117], v[30:31], off offset:128
	global_load_dwordx4 v[118:121], v[22:23], off offset:-64
	global_load_dwordx4 v[122:125], v[24:25], off offset:384
	global_load_dwordx4 v[126:129], v[24:25], off offset:400
	global_load_dwordx4 v[130:133], v[28:29], off offset:192
	global_load_dwordx4 v[134:137], v[30:31], off offset:192
	global_load_dwordx4 v[138:141], v[22:23], off
	global_load_dwordx4 v[142:145], v[24:25], off offset:512
	global_load_dwordx4 v[146:149], v[24:25], off offset:528
	global_load_dwordx4 v[150:153], v[28:29], off offset:256
	global_load_dwordx4 v[154:157], v[22:23], off offset:64
	global_load_dwordx4 v[158:161], v[24:25], off offset:656
	global_load_dwordx4 v[162:165], v[24:25], off offset:640
	global_load_dwordx4 v[166:169], v[30:31], off offset:256
	global_load_dwordx4 v[170:173], v[28:29], off offset:320
	global_load_dwordx4 v[174:177], v[22:23], off offset:128
	global_load_dwordx4 v[178:181], v[24:25], off offset:784
	global_load_dwordx4 v[182:185], v[24:25], off offset:768
	global_load_dwordx4 v[186:189], v[30:31], off offset:320
	global_load_dwordx4 v[190:193], v[22:23], off offset:192
	global_load_dwordx4 v[194:197], v[24:25], off offset:912
	global_load_dwordx4 v[198:201], v[24:25], off offset:896
	global_load_dwordx4 v[202:205], v[28:29], off offset:384
	global_load_dwordx4 v[206:209], v[30:31], off offset:384
	global_load_dwordx4 v[210:213], v[28:29], off offset:448
	global_load_dwordx4 v[214:217], v[30:31], off offset:448
	v_mov_b32_e32 v55, 0
	v_mov_b32_e32 v56, 0
	v_mov_b32_e32 v57, 0
	v_mov_b32_e32 v58, 0
	v_mov_b32_e32 v59, 0
	v_mov_b32_e32 v60, 0
	v_mov_b32_e32 v61, 0
	s_add_u32 s12, s12, 0x400
	s_addc_u32 s13, s13, 0
	v_lshl_add_u64 v[10:11], v[10:11], 0, s[14:15]
	v_lshl_add_u64 v[14:15], v[14:15], 0, s[14:15]
	s_cmpk_eq_i32 s12, 0x1000
	v_lshl_add_u64 v[16:17], v[16:17], 0, s[16:17]
	s_waitcnt vmcnt(39)
	v_cvt_f32_f16_e32 v48, v34
	v_cvt_f32_f16_sdwa v49, v34 dst_sel:DWORD dst_unused:UNUSED_PAD src0_sel:WORD_1
	v_cvt_f32_f16_e32 v34, v35
	v_cvt_f32_f16_sdwa v35, v35 dst_sel:DWORD dst_unused:UNUSED_PAD src0_sel:WORD_1
	v_cvt_f32_f16_e32 v50, v36
	v_cvt_f32_f16_sdwa v51, v36 dst_sel:DWORD dst_unused:UNUSED_PAD src0_sel:WORD_1
	v_cvt_f32_f16_e32 v52, v37
	v_cvt_f32_f16_sdwa v53, v37 dst_sel:DWORD dst_unused:UNUSED_PAD src0_sel:WORD_1
	s_waitcnt vmcnt(38)
	v_pk_mul_f32 v[34:35], v[40:41], v[34:35]
	v_pk_mul_f32 v[36:37], v[38:39], v[48:49]
	s_waitcnt vmcnt(37)
	v_pk_mul_f32 v[40:41], v[42:43], v[50:51]
	v_pk_mul_f32 v[36:37], v[18:19], v[36:37]
	v_pk_mul_f32 v[40:41], v[18:19], v[40:41]
	v_cvt_pk_fp8_f32 v46, v36, v37
	v_cvt_pk_fp8_f32 v47, v40, v41
	v_pk_mul_f32 v[38:39], v[44:45], v[52:53]
	v_pk_mul_f32 v[42:43], v[20:21], v[34:35]
	v_pk_mul_f32 v[38:39], v[20:21], v[38:39]
	v_cvt_pk_fp8_f32 v46, v42, v43 op_sel:[0,0,1]
	v_cvt_pk_fp8_f32 v47, v38, v39 op_sel:[0,0,1]
	v_cvt_pk_f16_f32 v34, v36, v37
	v_cvt_pk_f16_f32 v35, v42, v43
	v_cvt_pk_f16_f32 v36, v40, v41
	global_store_dwordx2 v[26:27], v[46:47], off offset:-128
	v_cvt_pk_f16_f32 v37, v38, v39
	s_waitcnt vmcnt(36)
	v_mov_b32_e32 v38, v70
	v_mov_b32_e32 v39, v71
	v_mov_b32_e32 v40, v72
	v_mov_b32_e32 v41, v73
	s_waitcnt vmcnt(35)
	v_mov_b32_e32 v42, v74
	v_mov_b32_e32 v43, v75
	v_mov_b32_e32 v44, v76
	v_mov_b32_e32 v45, v77
	s_waitcnt vmcnt(34)
	v_mov_b32_e32 v46, v78
	v_mov_b32_e32 v47, v79
	v_mov_b32_e32 v48, v80
	v_mov_b32_e32 v49, v81
	s_waitcnt vmcnt(33)
	v_mov_b32_e32 v50, v82
	v_mov_b32_e32 v51, v83
	v_mov_b32_e32 v52, v84
	v_mov_b32_e32 v53, v85
	s_nop 0
	v_mfma_f32_16x16x32_f16 v[2:5], v[34:37], v[38:41], v[2:5]
	s_waitcnt vmcnt(32)
	v_mov_b32_e32 v38, v86
	v_mov_b32_e32 v39, v87
	v_mov_b32_e32 v40, v88
	v_mov_b32_e32 v41, v89
	s_nop 0
	v_mfma_f32_16x16x32_f16 v[6:9], v[34:37], v[42:45], v[6:9]
	s_nop 0
	v_cvt_f32_f16_e32 v34, v46
	v_cvt_f32_f16_sdwa v35, v46 dst_sel:DWORD dst_unused:UNUSED_PAD src0_sel:WORD_1
	v_cvt_f32_f16_e32 v36, v47
	v_cvt_f32_f16_sdwa v37, v47 dst_sel:DWORD dst_unused:UNUSED_PAD src0_sel:WORD_1
	v_cvt_f32_f16_e32 v42, v48
	v_cvt_f32_f16_sdwa v43, v48 dst_sel:DWORD dst_unused:UNUSED_PAD src0_sel:WORD_1
	v_cvt_f32_f16_e32 v44, v49
	v_cvt_f32_f16_sdwa v45, v49 dst_sel:DWORD dst_unused:UNUSED_PAD src0_sel:WORD_1
	s_nop 0
	v_pk_mul_f32 v[36:37], v[52:53], v[36:37]
	v_pk_mul_f32 v[34:35], v[50:51], v[34:35]
	s_nop 0
	v_pk_mul_f32 v[38:39], v[38:39], v[42:43]
	v_pk_mul_f32 v[42:43], v[20:21], v[36:37]
	v_pk_mul_f32 v[36:37], v[18:19], v[34:35]
	v_pk_mul_f32 v[38:39], v[18:19], v[38:39]
	v_cvt_pk_fp8_f32 v54, v36, v37
	v_cvt_pk_fp8_f32 v55, v38, v39
	v_pk_mul_f32 v[40:41], v[40:41], v[44:45]
	v_cvt_pk_f16_f32 v34, v36, v37
	v_pk_mul_f32 v[40:41], v[20:21], v[40:41]
	v_cvt_pk_fp8_f32 v54, v42, v43 op_sel:[0,0,1]
	v_cvt_pk_fp8_f32 v55, v40, v41 op_sel:[0,0,1]
	v_cvt_pk_f16_f32 v35, v42, v43
	v_cvt_pk_f16_f32 v36, v38, v39
	v_cvt_pk_f16_f32 v37, v40, v41
	global_store_dwordx2 v[26:27], v[54:55], off offset:-96
	s_waitcnt vmcnt(31)
	v_mov_b32_e32 v38, v90
	v_mov_b32_e32 v39, v91
	v_mov_b32_e32 v40, v92
	v_mov_b32_e32 v41, v93
	s_waitcnt vmcnt(30)
	v_mov_b32_e32 v42, v94
	v_mov_b32_e32 v43, v95
	v_mov_b32_e32 v44, v96
	v_mov_b32_e32 v45, v97
	s_waitcnt vmcnt(29)
	v_mov_b32_e32 v46, v98
	v_mov_b32_e32 v47, v99
	v_mov_b32_e32 v48, v100
	v_mov_b32_e32 v49, v101
	s_waitcnt vmcnt(28)
	v_mov_b32_e32 v50, v102
	v_mov_b32_e32 v51, v103
	v_mov_b32_e32 v52, v104
	v_mov_b32_e32 v53, v105
	v_mov_b32_e32 v54, 0
	v_mov_b32_e32 v55, 0
	s_nop 0
	v_mfma_f32_16x16x32_f16 v[2:5], v[34:37], v[38:41], v[2:5]
	s_waitcnt vmcnt(27)
	v_mov_b32_e32 v38, v106
	v_mov_b32_e32 v39, v107
	v_mov_b32_e32 v40, v108
	v_mov_b32_e32 v41, v109
	s_nop 0
	v_mfma_f32_16x16x32_f16 v[6:9], v[34:37], v[42:45], v[6:9]
	s_nop 0
	v_cvt_f32_f16_e32 v34, v46
	v_cvt_f32_f16_sdwa v35, v46 dst_sel:DWORD dst_unused:UNUSED_PAD src0_sel:WORD_1
	v_cvt_f32_f16_e32 v36, v47
	v_cvt_f32_f16_sdwa v37, v47 dst_sel:DWORD dst_unused:UNUSED_PAD src0_sel:WORD_1
	v_cvt_f32_f16_e32 v42, v48
	v_cvt_f32_f16_sdwa v43, v48 dst_sel:DWORD dst_unused:UNUSED_PAD src0_sel:WORD_1
	v_cvt_f32_f16_e32 v44, v49
	v_cvt_f32_f16_sdwa v45, v49 dst_sel:DWORD dst_unused:UNUSED_PAD src0_sel:WORD_1
	s_nop 0
	v_pk_mul_f32 v[36:37], v[52:53], v[36:37]
	v_pk_mul_f32 v[34:35], v[50:51], v[34:35]
	s_nop 0
	v_pk_mul_f32 v[38:39], v[38:39], v[42:43]
	v_pk_mul_f32 v[42:43], v[20:21], v[36:37]
	v_pk_mul_f32 v[36:37], v[18:19], v[34:35]
	v_pk_mul_f32 v[38:39], v[18:19], v[38:39]
	v_cvt_pk_fp8_f32 v56, v36, v37
	v_cvt_pk_fp8_f32 v57, v38, v39
	v_pk_mul_f32 v[40:41], v[40:41], v[44:45]
	v_cvt_pk_f16_f32 v34, v36, v37
	v_pk_mul_f32 v[40:41], v[20:21], v[40:41]
	v_cvt_pk_fp8_f32 v56, v42, v43 op_sel:[0,0,1]
	v_cvt_pk_fp8_f32 v57, v40, v41 op_sel:[0,0,1]
	v_cvt_pk_f16_f32 v35, v42, v43
	v_cvt_pk_f16_f32 v36, v38, v39
	v_cvt_pk_f16_f32 v37, v40, v41
	global_store_dwordx2 v[26:27], v[56:57], off offset:-64
	s_waitcnt vmcnt(26)
	v_mov_b32_e32 v38, v110
	v_mov_b32_e32 v39, v111
	v_mov_b32_e32 v40, v112
	v_mov_b32_e32 v41, v113
	s_waitcnt vmcnt(25)
	v_mov_b32_e32 v42, v114
	v_mov_b32_e32 v43, v115
	v_mov_b32_e32 v44, v116
	v_mov_b32_e32 v45, v117
	s_waitcnt vmcnt(24)
	v_mov_b32_e32 v46, v118
	v_mov_b32_e32 v47, v119
	v_mov_b32_e32 v48, v120
	v_mov_b32_e32 v49, v121
	s_waitcnt vmcnt(23)
	v_mov_b32_e32 v50, v122
	v_mov_b32_e32 v51, v123
	v_mov_b32_e32 v52, v124
	v_mov_b32_e32 v53, v125
	s_nop 0
	v_mfma_f32_16x16x32_f16 v[2:5], v[34:37], v[38:41], v[2:5]
	s_waitcnt vmcnt(22)
	v_mov_b32_e32 v38, v126
	v_mov_b32_e32 v39, v127
	v_mov_b32_e32 v40, v128
	v_mov_b32_e32 v41, v129
	s_nop 0
	v_mfma_f32_16x16x32_f16 v[6:9], v[34:37], v[42:45], v[6:9]
	s_nop 0
	v_cvt_f32_f16_e32 v34, v46
	v_cvt_f32_f16_sdwa v35, v46 dst_sel:DWORD dst_unused:UNUSED_PAD src0_sel:WORD_1
	v_cvt_f32_f16_e32 v36, v47
	v_cvt_f32_f16_sdwa v37, v47 dst_sel:DWORD dst_unused:UNUSED_PAD src0_sel:WORD_1
	v_cvt_f32_f16_e32 v42, v48
	v_cvt_f32_f16_sdwa v43, v48 dst_sel:DWORD dst_unused:UNUSED_PAD src0_sel:WORD_1
	v_cvt_f32_f16_e32 v44, v49
	v_cvt_f32_f16_sdwa v45, v49 dst_sel:DWORD dst_unused:UNUSED_PAD src0_sel:WORD_1
	s_nop 0
	v_pk_mul_f32 v[36:37], v[52:53], v[36:37]
	v_pk_mul_f32 v[34:35], v[50:51], v[34:35]
	s_nop 0
	v_pk_mul_f32 v[38:39], v[38:39], v[42:43]
	v_pk_mul_f32 v[42:43], v[20:21], v[36:37]
	v_pk_mul_f32 v[36:37], v[18:19], v[34:35]
	v_pk_mul_f32 v[38:39], v[18:19], v[38:39]
	v_cvt_pk_fp8_f32 v58, v36, v37
	v_cvt_pk_fp8_f32 v59, v38, v39
	v_pk_mul_f32 v[40:41], v[40:41], v[44:45]
	v_cvt_pk_f16_f32 v34, v36, v37
	v_pk_mul_f32 v[40:41], v[20:21], v[40:41]
	v_cvt_pk_fp8_f32 v58, v42, v43 op_sel:[0,0,1]
	v_cvt_pk_fp8_f32 v59, v40, v41 op_sel:[0,0,1]
	v_cvt_pk_f16_f32 v35, v42, v43
	v_cvt_pk_f16_f32 v36, v38, v39
	v_cvt_pk_f16_f32 v37, v40, v41
	global_store_dwordx2 v[26:27], v[58:59], off offset:-32
	s_waitcnt vmcnt(21)
	v_mov_b32_e32 v38, v130
	v_mov_b32_e32 v39, v131
	v_mov_b32_e32 v40, v132
	v_mov_b32_e32 v41, v133
	s_waitcnt vmcnt(20)
	v_mov_b32_e32 v42, v134
	v_mov_b32_e32 v43, v135
	v_mov_b32_e32 v44, v136
	v_mov_b32_e32 v45, v137
	s_waitcnt vmcnt(19)
	v_mov_b32_e32 v46, v138
	v_mov_b32_e32 v47, v139
	v_mov_b32_e32 v48, v140
	v_mov_b32_e32 v49, v141
	s_waitcnt vmcnt(18)
	v_mov_b32_e32 v50, v142
	v_mov_b32_e32 v51, v143
	v_mov_b32_e32 v52, v144
	v_mov_b32_e32 v53, v145
	v_mov_b32_e32 v58, 0
	v_mov_b32_e32 v59, 0
	s_nop 0
	v_mfma_f32_16x16x32_f16 v[2:5], v[34:37], v[38:41], v[2:5]
	s_waitcnt vmcnt(17)
	v_mov_b32_e32 v38, v146
	v_mov_b32_e32 v39, v147
	v_mov_b32_e32 v40, v148
	v_mov_b32_e32 v41, v149
	s_nop 0
	v_mfma_f32_16x16x32_f16 v[6:9], v[34:37], v[42:45], v[6:9]
	s_nop 0
	v_cvt_f32_f16_e32 v34, v46
	v_cvt_f32_f16_sdwa v35, v46 dst_sel:DWORD dst_unused:UNUSED_PAD src0_sel:WORD_1
	v_cvt_f32_f16_e32 v36, v47
	v_cvt_f32_f16_sdwa v37, v47 dst_sel:DWORD dst_unused:UNUSED_PAD src0_sel:WORD_1
	v_cvt_f32_f16_e32 v42, v48
	v_cvt_f32_f16_sdwa v43, v48 dst_sel:DWORD dst_unused:UNUSED_PAD src0_sel:WORD_1
	v_cvt_f32_f16_e32 v44, v49
	v_cvt_f32_f16_sdwa v45, v49 dst_sel:DWORD dst_unused:UNUSED_PAD src0_sel:WORD_1
	s_nop 0
	v_pk_mul_f32 v[36:37], v[52:53], v[36:37]
	v_pk_mul_f32 v[34:35], v[50:51], v[34:35]
	s_nop 0
	v_pk_mul_f32 v[38:39], v[38:39], v[42:43]
	v_pk_mul_f32 v[42:43], v[20:21], v[36:37]
	v_pk_mul_f32 v[36:37], v[18:19], v[34:35]
	v_pk_mul_f32 v[38:39], v[18:19], v[38:39]
	v_cvt_pk_fp8_f32 v54, v36, v37
	v_cvt_pk_fp8_f32 v55, v38, v39
	v_pk_mul_f32 v[40:41], v[40:41], v[44:45]
	v_cvt_pk_f16_f32 v34, v36, v37
	v_pk_mul_f32 v[40:41], v[20:21], v[40:41]
	v_cvt_pk_fp8_f32 v54, v42, v43 op_sel:[0,0,1]
	v_cvt_pk_fp8_f32 v55, v40, v41 op_sel:[0,0,1]
	v_cvt_pk_f16_f32 v35, v42, v43
	v_cvt_pk_f16_f32 v36, v38, v39
	v_cvt_pk_f16_f32 v37, v40, v41
	global_store_dwordx2 v[26:27], v[54:55], off
	s_waitcnt vmcnt(16)
	v_mov_b32_e32 v38, v150
	v_mov_b32_e32 v39, v151
	v_mov_b32_e32 v40, v152
	v_mov_b32_e32 v41, v153
	s_waitcnt vmcnt(15)
	v_mov_b32_e32 v42, v154
	v_mov_b32_e32 v43, v155
	v_mov_b32_e32 v44, v156
	v_mov_b32_e32 v45, v157
	s_waitcnt vmcnt(14)
	v_mov_b32_e32 v46, v158
	v_mov_b32_e32 v47, v159
	v_mov_b32_e32 v48, v160
	v_mov_b32_e32 v49, v161
	s_waitcnt vmcnt(13)
	v_mov_b32_e32 v50, v162
	v_mov_b32_e32 v51, v163
	v_mov_b32_e32 v52, v164
	v_mov_b32_e32 v53, v165
	s_nop 0
	s_waitcnt vmcnt(12)
	v_mov_b32_e32 v54, v166
	v_mov_b32_e32 v55, v167
	v_mov_b32_e32 v56, v168
	v_mov_b32_e32 v57, v169
	s_nop 0
	v_mfma_f32_16x16x32_f16 v[2:5], v[34:37], v[38:41], v[2:5]
	s_nop 0
	v_cvt_f32_f16_e32 v40, v44
	v_cvt_f32_f16_sdwa v41, v44 dst_sel:DWORD dst_unused:UNUSED_PAD src0_sel:WORD_1
	v_mov_b32_e32 v38, 0
	s_nop 0
	v_mfma_f32_16x16x32_f16 v[6:9], v[34:37], v[54:57], v[6:9]
	v_cvt_f32_f16_e32 v34, v42
	v_cvt_f32_f16_sdwa v35, v42 dst_sel:DWORD dst_unused:UNUSED_PAD src0_sel:WORD_1
	v_cvt_f32_f16_e32 v36, v43
	v_cvt_f32_f16_sdwa v37, v43 dst_sel:DWORD dst_unused:UNUSED_PAD src0_sel:WORD_1
	v_cvt_f32_f16_e32 v42, v45
	v_cvt_f32_f16_sdwa v43, v45 dst_sel:DWORD dst_unused:UNUSED_PAD src0_sel:WORD_1
	v_pk_mul_f32 v[34:35], v[50:51], v[34:35]
	v_pk_mul_f32 v[36:37], v[52:53], v[36:37]
	v_pk_mul_f32 v[40:41], v[46:47], v[40:41]
	v_mov_b32_e32 v39, 0
	v_pk_mul_f32 v[44:45], v[20:21], v[36:37]
	v_pk_mul_f32 v[36:37], v[18:19], v[34:35]
	v_pk_mul_f32 v[40:41], v[18:19], v[40:41]
	v_cvt_pk_fp8_f32 v38, v36, v37
	v_cvt_pk_fp8_f32 v39, v40, v41
	v_pk_mul_f32 v[42:43], v[48:49], v[42:43]
	v_cvt_pk_f16_f32 v34, v36, v37
	v_pk_mul_f32 v[42:43], v[20:21], v[42:43]
	v_cvt_pk_fp8_f32 v38, v44, v45 op_sel:[0,0,1]
	v_cvt_pk_fp8_f32 v39, v42, v43 op_sel:[0,0,1]
	v_cvt_pk_f16_f32 v35, v44, v45
	v_cvt_pk_f16_f32 v36, v40, v41
	v_cvt_pk_f16_f32 v37, v42, v43
	global_store_dwordx2 v[26:27], v[38:39], off offset:32
	s_waitcnt vmcnt(11)
	v_mov_b32_e32 v38, v170
	v_mov_b32_e32 v39, v171
	v_mov_b32_e32 v40, v172
	v_mov_b32_e32 v41, v173
	s_nop 0
	s_waitcnt vmcnt(10)
	v_mov_b32_e32 v42, v174
	v_mov_b32_e32 v43, v175
	v_mov_b32_e32 v44, v176
	v_mov_b32_e32 v45, v177
	s_waitcnt vmcnt(9)
	v_mov_b32_e32 v46, v178
	v_mov_b32_e32 v47, v179
	v_mov_b32_e32 v48, v180
	v_mov_b32_e32 v49, v181
	s_waitcnt vmcnt(8)
	v_mov_b32_e32 v50, v182
	v_mov_b32_e32 v51, v183
	v_mov_b32_e32 v52, v184
	v_mov_b32_e32 v53, v185
	s_waitcnt vmcnt(7)
	v_mov_b32_e32 v54, v186
	v_mov_b32_e32 v55, v187
	v_mov_b32_e32 v56, v188
	v_mov_b32_e32 v57, v189
	s_nop 0
	v_mfma_f32_16x16x32_f16 v[2:5], v[34:37], v[38:41], v[2:5]
	s_nop 0
	v_cvt_f32_f16_e32 v38, v44
	v_cvt_f32_f16_sdwa v39, v44 dst_sel:DWORD dst_unused:UNUSED_PAD src0_sel:WORD_1
	v_cvt_f32_f16_e32 v40, v45
	s_nop 0
	v_mfma_f32_16x16x32_f16 v[6:9], v[34:37], v[54:57], v[6:9]
	v_cvt_f32_f16_e32 v34, v42
	v_cvt_f32_f16_sdwa v35, v42 dst_sel:DWORD dst_unused:UNUSED_PAD src0_sel:WORD_1
	v_cvt_f32_f16_e32 v36, v43
	v_cvt_f32_f16_sdwa v37, v43 dst_sel:DWORD dst_unused:UNUSED_PAD src0_sel:WORD_1
	v_cvt_f32_f16_sdwa v41, v45 dst_sel:DWORD dst_unused:UNUSED_PAD src0_sel:WORD_1
	v_pk_mul_f32 v[34:35], v[50:51], v[34:35]
	v_pk_mul_f32 v[38:39], v[46:47], v[38:39]
	v_pk_mul_f32 v[36:37], v[52:53], v[36:37]
	v_pk_mul_f32 v[38:39], v[18:19], v[38:39]
	v_pk_mul_f32 v[42:43], v[20:21], v[36:37]
	v_pk_mul_f32 v[36:37], v[18:19], v[34:35]
	v_cvt_pk_fp8_f32 v59, v38, v39
	v_cvt_pk_fp8_f32 v58, v36, v37
	v_pk_mul_f32 v[40:41], v[48:49], v[40:41]
	v_cvt_pk_f16_f32 v34, v36, v37
	v_pk_mul_f32 v[40:41], v[20:21], v[40:41]
	v_cvt_pk_fp8_f32 v58, v42, v43 op_sel:[0,0,1]
	v_cvt_pk_fp8_f32 v59, v40, v41 op_sel:[0,0,1]
	v_cvt_pk_f16_f32 v35, v42, v43
	v_cvt_pk_f16_f32 v36, v38, v39
	v_cvt_pk_f16_f32 v37, v40, v41
	global_store_dwordx2 v[26:27], v[58:59], off offset:64
	s_waitcnt vmcnt(6)
	v_mov_b32_e32 v38, v190
	v_mov_b32_e32 v39, v191
	v_mov_b32_e32 v40, v192
	v_mov_b32_e32 v41, v193
	s_waitcnt vmcnt(5)
	v_mov_b32_e32 v42, v194
	v_mov_b32_e32 v43, v195
	v_mov_b32_e32 v44, v196
	v_mov_b32_e32 v45, v197
	s_waitcnt vmcnt(4)
	v_mov_b32_e32 v46, v198
	v_mov_b32_e32 v47, v199
	v_mov_b32_e32 v48, v200
	v_mov_b32_e32 v49, v201
	s_waitcnt vmcnt(3)
	v_mov_b32_e32 v50, v202
	v_mov_b32_e32 v51, v203
	v_mov_b32_e32 v52, v204
	v_mov_b32_e32 v53, v205
	s_waitcnt vmcnt(2)
	v_mov_b32_e32 v54, v206
	v_mov_b32_e32 v55, v207
	v_mov_b32_e32 v56, v208
	v_mov_b32_e32 v57, v209
	s_nop 0
	v_mfma_f32_16x16x32_f16 v[2:5], v[34:37], v[50:53], v[2:5]
	v_cvt_f32_f16_e32 v22, v38
	v_cvt_f32_f16_sdwa v23, v38 dst_sel:DWORD dst_unused:UNUSED_PAD src0_sel:WORD_1
	v_cvt_f32_f16_e32 v24, v39
	v_cvt_f32_f16_sdwa v25, v39 dst_sel:DWORD dst_unused:UNUSED_PAD src0_sel:WORD_1
	v_cvt_f32_f16_e32 v38, v40
	v_cvt_f32_f16_sdwa v39, v40 dst_sel:DWORD dst_unused:UNUSED_PAD src0_sel:WORD_1
	v_cvt_f32_f16_e32 v50, v41
	v_cvt_f32_f16_sdwa v51, v41 dst_sel:DWORD dst_unused:UNUSED_PAD src0_sel:WORD_1
	v_pk_mul_f32 v[22:23], v[46:47], v[22:23]
	v_pk_mul_f32 v[38:39], v[42:43], v[38:39]
	v_pk_mul_f32 v[24:25], v[48:49], v[24:25]
	v_pk_mul_f32 v[40:41], v[44:45], v[50:51]
	v_pk_mul_f32 v[44:45], v[18:19], v[22:23]
	v_pk_mul_f32 v[48:49], v[18:19], v[38:39]
	v_cvt_pk_fp8_f32 v60, v44, v45
	v_cvt_pk_fp8_f32 v61, v48, v49
	v_pk_mul_f32 v[42:43], v[20:21], v[24:25]
	v_pk_mul_f32 v[46:47], v[20:21], v[40:41]
	v_cvt_pk_fp8_f32 v60, v42, v43 op_sel:[0,0,1]
	v_cvt_pk_fp8_f32 v61, v46, v47 op_sel:[0,0,1]
	s_nop 0
	v_mfma_f32_16x16x32_f16 v[6:9], v[34:37], v[54:57], v[6:9]
	global_store_dwordx2 v[26:27], v[60:61], off offset:96
	s_waitcnt vmcnt(1)
	v_mov_b32_e32 v22, v210
	v_mov_b32_e32 v23, v211
	v_mov_b32_e32 v24, v212
	v_mov_b32_e32 v25, v213
	s_waitcnt vmcnt(0)
	v_mov_b32_e32 v38, v214
	v_mov_b32_e32 v39, v215
	v_mov_b32_e32 v40, v216
	v_mov_b32_e32 v41, v217
	v_cvt_pk_f16_f32 v26, v44, v45
	v_cvt_pk_f16_f32 v27, v42, v43
	v_cvt_pk_f16_f32 v28, v48, v49
	v_cvt_pk_f16_f32 v29, v46, v47
	s_nop 0
	s_nop 0
	v_mfma_f32_16x16x32_f16 v[2:5], v[26:29], v[22:25], v[2:5]
	s_nop 0
	v_mfma_f32_16x16x32_f16 v[6:9], v[26:29], v[38:41], v[6:9]
	s_cbranch_scc0 .LBB0_1272
	s_lshl_b32 s4, s20, 11
	s_add_i32 s4, s4, 0
	v_lshlrev_b32_e32 v10, 5, v33
	s_cmp_eq_u32 s19, 1
	v_add_u32_e32 v10, s4, v10
	s_cbranch_scc0 .LBB0_1275
	ds_write_b128 v10, v[2:5] offset:16896
	ds_write_b128 v10, v[6:9] offset:16912
